# v066
# speedup vs baseline: 1.0071x; 1.0071x over previous
.Ltok_done:
	v_cmp_ne_u32_e32 vcc, 0, v7
	s_and_saveexec_b64 s[6:7], vcc
	v_mov_b32_e32 v1, 1
	v_mov_b32_e32 v2, 0
	ds_write_b32 v2, v1 offset:24832
	s_or_b64 exec, exec, s[6:7]
	s_mov_b32 s5, 0
	s_cmp_eq_u32 s16, 0
	s_cselect_b64 vcc, -1, 0
	v_mov_b32_e32 v157, 0
	s_waitcnt lgkmcnt(0)
	s_barrier
	ds_read_b32 v1, v157 offset:24832
	v_lshrrev_b32_e32 v108, 6, v0
	v_and_b32_e32 v4, 63, v0
	s_movk_i32 s0, 0x1000
	v_mov_b32_e32 v9, v157
	s_waitcnt lgkmcnt(0)
	v_readfirstlane_b32 s4, v1
	v_lshl_or_b32 v1, s16, 3, v108
	v_mul_u32_u24_e32 v1, 0x300, v1
	v_lshlrev_b32_e32 v156, 4, v1
	v_lshl_add_u64 v[2:3], s[8:9], 0, v[156:157]
	v_lshlrev_b32_e32 v156, 4, v4
	v_lshl_add_u64 v[2:3], v[2:3], 0, v[156:157]
	v_add_co_u32_e64 v4, s[0:1], s0, v2
	v_lshl_or_b32 v1, s16, 4, v108
	s_nop 0
	v_addc_co_u32_e64 v5, s[0:1], 0, v3, s[0:1]
	s_movk_i32 s0, 0x2000
	s_nop 0
	v_add_co_u32_e64 v6, s[0:1], s0, v2
	v_or_b32_e32 v8, 8, v1
	s_nop 0
	v_addc_co_u32_e64 v7, s[0:1], 0, v3, s[0:1]
	s_add_u32 s0, s8, 0x30000
	v_mul_u32_u24_e32 v8, 0xc0, v8
	s_addc_u32 s1, s9, 0
	v_lshlrev_b32_e32 v8, 4, v8
	v_mul_u32_u24_e32 v1, 0xc0, v1
	v_lshl_add_u64 v[92:93], s[0:1], 0, v[8:9]
	v_lshlrev_b32_e32 v8, 4, v1
	s_cmp_lg_u32 s4, 0
	v_lshl_add_u64 v[8:9], s[0:1], 0, v[8:9]
	s_cselect_b64 s[12:13], -1, 0
	s_lshl_b32 s0, s16, 11
	s_add_u32 s0, s8, s0
	s_addc_u32 s1, s9, 0
	v_and_b32_e32 v10, 0x1c0, v0
	v_mov_b32_e32 v11, v157
	v_lshl_add_u64 v[10:11], s[0:1], 0, v[10:11]
	v_and_b32_e32 v12, 48, v0
	v_mov_b32_e32 v13, v157
	v_and_b32_e32 v161, 15, v0
	v_lshl_add_u64 v[10:11], v[10:11], 0, v[12:13]
	s_mov_b64 s[0:1], 0x48000
	v_lshrrev_b32_e32 v12, 5, v0
	v_bfe_u32 v13, v0, 5, 1
	v_bfe_u32 v109, v0, 4, 2
	v_lshl_add_u64 v[72:73], v[10:11], 0, s[0:1]
	s_mov_b32 s0, 0x48000
	v_lshlrev_b32_e32 v1, 3, v0
	v_and_or_b32 v12, v12, 2, v13
	v_lshlrev_b32_e32 v13, 4, v161
	v_lshrrev_b32_e32 v0, 1, v0
	v_add_co_u32_e64 v10, s[0:1], s0, v10
	v_and_b32_e32 v1, 0xc00, v1
	v_lshl_or_b32 v12, v12, 8, v13
	v_and_b32_e32 v0, 8, v0
	v_lshl_add_u64 v[8:9], v[8:9], 0, v[156:157]
	v_addc_co_u32_e64 v11, s[0:1], 0, v11, s[0:1]
	v_or3_b32 v163, v12, v1, v0
	global_load_dwordx4 v[12:15], v[2:3], off
	global_load_dwordx4 v[16:19], v[2:3], off offset:1024
	global_load_dwordx4 v[20:23], v[2:3], off offset:2048
	global_load_dwordx4 v[24:27], v[2:3], off offset:3072
	global_load_dwordx4 v[28:31], v[6:7], off offset:-4096
	global_load_dwordx4 v[32:35], v[6:7], off
	global_load_dwordx4 v[36:39], v[6:7], off offset:1024
	global_load_dwordx4 v[40:43], v[6:7], off offset:2048
	global_load_dwordx4 v[44:47], v[6:7], off offset:3072
	global_load_dwordx4 v[48:51], v[4:5], off offset:1024
	global_load_dwordx4 v[52:55], v[4:5], off offset:2048
	global_load_dwordx4 v[56:59], v[4:5], off offset:3072
	global_load_dwordx4 v[60:63], v[8:9], off
	global_load_dwordx4 v[64:67], v[8:9], off offset:1024
	global_load_dwordx4 v[68:71], v[8:9], off offset:2048
	global_load_dwordx4 v[76:79], v[72:73], off offset:512
	global_load_dwordx4 v[80:83], v[72:73], off offset:1024
	global_load_dwordx4 v[84:87], v[10:11], off
	global_load_dwordx4 v[88:91], v[72:73], off offset:1536
	s_and_b64 s[0:1], vcc, exec
	s_cselect_b32 s14, 0, 0x7f
	s_lshl_b32 s7, s16, 22
	s_add_u32 s0, s8, s7
	s_addc_u32 s1, s9, 0
	v_lshlrev_b32_e32 v94, 12, v108
	v_mov_b32_e32 v95, v157
	v_lshl_add_u64 v[0:1], s[0:1], 0, v[94:95]
	v_lshl_add_u64 v[0:1], v[0:1], 0, v[156:157]
	s_mov_b64 s[0:1], 0xc9000
	v_lshl_add_u64 v[158:159], v[0:1], 0, s[0:1]
	s_lshl_b32 s4, s14, 15
	v_lshl_add_u64 v[96:97], v[158:159], 0, s[4:5]
	global_load_dwordx4 v[72:75], v[96:97], off
	global_load_dwordx4 v[8:11], v[96:97], off offset:1024
	global_load_dwordx4 v[4:7], v[96:97], off offset:2048
	global_load_dwordx4 v[0:3], v[96:97], off offset:3072
	v_mul_u32_u24_e32 v95, 0x104, v161
	ds_read_b32 v96, v95 offset:16512
	ds_read_b32 v95, v95 offset:20672
	s_movk_i32 s6, 0x410
	s_movk_i32 s0, 0x104
	v_mov_b32_e32 v97, 0x4080
	s_waitcnt lgkmcnt(1)
	v_lshrrev_b32_e32 v178, 16, v96
	v_and_b32_e32 v96, 0xffff, v96
	v_mad_u32_u24 v176, v161, s0, v97
	v_mad_u32_u24 v110, v109, s6, v96
	s_waitcnt lgkmcnt(0)
	v_lshrrev_b32_e32 v177, 16, v95
	v_and_b32_e32 v95, 0xffff, v95
	s_and_b64 s[0:1], vcc, exec
	v_mad_u32_u24 v111, v109, s6, v95
	s_cselect_b32 s15, 1, -1
	s_or_b32 s0, s7, s4
	ds_read_b128 v[120:123], v110 offset:8192
	ds_read_b128 v[116:119], v111 offset:8192
	v_lshl_add_u64 v[164:165], v[92:93], 0, v[156:157]
	v_or3_b32 v92, s0, v94, v156
	v_mov_b32_e32 v93, v157
	v_lshl_add_u64 v[92:93], s[8:9], 0, v[92:93]
	s_mov_b64 s[0:1], 0xc9800
	s_lshl_b32 s4, s15, 1
	v_mov_b32_e32 v106, v157
	v_mov_b32_e32 v107, v157
	v_lshl_add_u64 v[166:167], v[92:93], 0, s[0:1]
	s_ashr_i32 s5, s4, 31
	v_mov_b32_e32 v100, 0xc47a0000
	v_mov_b32_e32 v104, v157
	v_mov_b32_e32 v105, v157
	v_cndmask_b32_e64 v92, 0, 1, s[12:13]
	v_mov_b64_e32 v[142:143], v[106:107]
	s_lshl_b64 s[6:7], s[4:5], 15
	s_add_i32 s8, s14, s15
	v_mov_b32_e32 v101, v100
	v_mov_b32_e32 v102, v100
	v_mov_b32_e32 v103, v100
	s_mov_b32 s5, -2
	v_cmp_ne_u32_e64 s[0:1], 1, v92
	v_mov_b32_e32 v172, v157
	v_mov_b32_e32 v173, v157
	v_mov_b32_e32 v174, v157
	v_mov_b32_e32 v175, v157
	v_mov_b32_e32 v96, v157
	v_mov_b32_e32 v97, v157
	v_mov_b32_e32 v98, v157
	v_mov_b32_e32 v99, v157
	v_mov_b32_e32 v92, v157
	v_mov_b32_e32 v93, v157
	v_mov_b32_e32 v94, v157
	v_mov_b32_e32 v95, v157
	v_mov_b32_e32 v144, v157
	v_mov_b32_e32 v145, v157
	v_mov_b32_e32 v146, v157
	v_mov_b32_e32 v147, v157
	v_mov_b32_e32 v132, v157
	v_mov_b32_e32 v133, v157
	v_mov_b32_e32 v134, v157
	v_mov_b32_e32 v135, v157
	v_mov_b32_e32 v128, v157
	v_mov_b32_e32 v129, v157
	v_mov_b32_e32 v130, v157
	v_mov_b32_e32 v131, v157
	v_mov_b32_e32 v136, v157
	v_mov_b32_e32 v137, v157
	v_mov_b32_e32 v138, v157
	v_mov_b32_e32 v139, v157
	v_mov_b32_e32 v124, v157
	v_mov_b32_e32 v125, v157
	v_mov_b32_e32 v126, v157
	v_mov_b32_e32 v127, v157
	v_mov_b32_e32 v170, v157
	v_mov_b32_e32 v171, v157
	v_mov_b32_e32 v168, v157
	v_mov_b32_e32 v169, v157
	v_lshlrev_b32_e32 v162, 4, v108
	v_mul_u32_u24_e32 v157, 0x410, v109
	v_lshlrev_b32_e32 v160, 2, v109
	v_mov_b64_e32 v[140:141], v[104:105]
	v_mov_b32_e32 v144, 0
	v_mov_b32_e32 v145, 0
	v_mov_b32_e32 v146, 0
	v_mov_b32_e32 v147, 0
	v_mov_b32_e32 v148, 0xc47a0000
	v_mov_b32_e32 v149, 0xc47a0000
	v_mov_b32_e32 v150, 0xc47a0000
	v_mov_b32_e32 v151, 0xc47a0000
	v_mov_b32_e32 v152, 0
	v_mov_b32_e32 v153, 0
	v_mov_b32_e32 v154, 0
	v_mov_b32_e32 v155, 0
	s_movk_i32 s17, 0x61
	global_load_dwordx4 v[206:209], v[164:165], off
	global_load_dwordx4 v[210:213], v[164:165], off offset:1024
	global_load_dwordx4 v[214:217], v[164:165], off offset:2048
	v_add_u32_e32 v226, v162, v160
	v_mul_u32_u24_e32 v226, 12, v226
	v_lshl_add_u32 v229, v161, 4, v157
	v_mul_u32_u24_e32 v230, 0x610, v161
	v_add_u32_e32 v230, v230, v226
	v_add_u32_e32 v231, 0x18400, v226
	s_waitcnt vmcnt(0) lgkmcnt(0)
	ds_read_b128 v[190:193], v229 offset:8192
	s_waitcnt lgkmcnt(0)
	v_mfma_f32_16x16x32_f16 v[194:197], v[60:63], v[190:193], v[84:87]
	v_mfma_f32_16x16x32_f16 v[198:201], v[64:67], v[190:193], v[76:79]
	v_mfma_f32_16x16x32_f16 v[202:205], v[68:71], v[190:193], v[88:91]
	s_nop 7
	s_nop 1
	ds_write_b128 v230, v[194:197] offset:24848
	ds_write_b128 v230, v[198:201] offset:24864
	ds_write_b128 v230, v[202:205] offset:24880
	v_add_u32_e32 v230, 0x6100, v230
	ds_read_b128 v[190:193], v229 offset:8448
	s_waitcnt lgkmcnt(0)
	v_mfma_f32_16x16x32_f16 v[194:197], v[60:63], v[190:193], v[84:87]
	v_mfma_f32_16x16x32_f16 v[198:201], v[64:67], v[190:193], v[76:79]
	v_mfma_f32_16x16x32_f16 v[202:205], v[68:71], v[190:193], v[88:91]
	s_nop 7
	s_nop 1
	ds_write_b128 v230, v[194:197] offset:24848
	ds_write_b128 v230, v[198:201] offset:24864
	ds_write_b128 v230, v[202:205] offset:24880
	v_add_u32_e32 v230, 0x6100, v230
	ds_read_b128 v[190:193], v229 offset:12864
	s_waitcnt lgkmcnt(0)
	v_mfma_f32_16x16x32_f16 v[194:197], v[206:209], v[190:193], v[84:87]
	v_mfma_f32_16x16x32_f16 v[198:201], v[210:213], v[190:193], v[76:79]
	v_mfma_f32_16x16x32_f16 v[202:205], v[214:217], v[190:193], v[88:91]
	s_nop 7
	s_nop 1
	ds_write_b128 v230, v[194:197] offset:24848
	ds_write_b128 v230, v[198:201] offset:24864
	ds_write_b128 v230, v[202:205] offset:24880
	v_add_u32_e32 v230, 0x6100, v230
	ds_read_b128 v[190:193], v229 offset:13120
	s_waitcnt lgkmcnt(0)
	v_mfma_f32_16x16x32_f16 v[194:197], v[206:209], v[190:193], v[84:87]
	v_mfma_f32_16x16x32_f16 v[198:201], v[210:213], v[190:193], v[76:79]
	v_mfma_f32_16x16x32_f16 v[202:205], v[214:217], v[190:193], v[88:91]
	s_nop 7
	s_nop 1
	ds_write_b128 v230, v[194:197] offset:24848
	ds_write_b128 v230, v[198:201] offset:24864
	ds_write_b128 v230, v[202:205] offset:24880
	ds_write_b128 v231, v[84:87] offset:24848
	ds_write_b128 v231, v[76:79] offset:24864
	ds_write_b128 v231, v[88:91] offset:24880
	ds_read_u16 v232, v176
	ds_read_u16 v177, v176 offset:4160
	s_waitcnt lgkmcnt(0)
	v_mad_u32_u24 v227, v232, s17, v226
	ds_read_b128 v[116:119], v227 offset:24848
	ds_read_b128 v[120:123], v227 offset:24864
	ds_read_b128 v[138:141], v227 offset:24880
	v_mov_b32_e32 v182, 0
	v_mov_b32_e32 v183, 0
	v_mov_b32_e32 v184, 0
	v_mov_b32_e32 v185, 0
	v_mov_b32_e32 v222, 0
	v_mov_b32_e32 v223, 0
	v_mov_b32_e32 v224, 0
	v_mov_b32_e32 v225, 0
	v_mov_b32_e32 v186, 0
	v_mov_b32_e32 v187, 0
	v_mov_b32_e32 v188, 0
	v_mov_b32_e32 v189, 0
	v_mov_b32_e32 v100, 0
	v_mov_b32_e32 v101, 0
	v_mov_b32_e32 v102, 0
	v_mov_b32_e32 v103, 0
	v_mov_b32_e32 v104, 0
	v_mov_b32_e32 v105, 0
	v_mov_b32_e32 v106, 0
	v_mov_b32_e32 v107, 0
	v_mov_b32_e32 v108, 0
	v_mov_b32_e32 v109, 0
	v_mov_b32_e32 v110, 0
	v_mov_b32_e32 v111, 0
	v_mov_b32_e32 v112, 0
	v_mov_b32_e32 v113, 0
	v_mov_b32_e32 v114, 0
	v_mov_b32_e32 v115, 0
	v_mov_b32_e32 v206, 0
	v_mov_b32_e32 v207, 0
	v_mov_b32_e32 v208, 0
	v_mov_b32_e32 v209, 0
	v_mov_b32_e32 v210, 0
	v_mov_b32_e32 v211, 0
	v_mov_b32_e32 v212, 0
	v_mov_b32_e32 v213, 0
	v_mov_b32_e32 v214, 0
	v_mov_b32_e32 v215, 0
	v_mov_b32_e32 v216, 0
	v_mov_b32_e32 v217, 0
	v_mov_b32_e32 v218, 0
	v_mov_b32_e32 v219, 0
	v_mov_b32_e32 v220, 0
	v_mov_b32_e32 v221, 0
	s_waitcnt vmcnt(4) lgkmcnt(0)
	v_readfirstlane_b32 s18, v162
	s_nop 3
	s_cmp_ge_u32 s18, 64
	s_cbranch_scc1 .Lgru_loop_b
	s_nop 0
